# speedup vs baseline: 1.0143x; 1.0074x over previous
_Z11attn_kernelPKDF16_S0_S0_PDF16_:
	s_bfe_u32 s26, s2, 0x20003
	s_load_dwordx8 s[4:11], s[0:1], 0x0
	s_lshr_b32 s1, s2, 2
	s_lshr_b32 s20, s2, 6
	v_readfirstlane_b32 s19, v0
	s_mov_b32 s21, 0
	s_lshl_b32 s27, s26, 8
	s_and_b32 s0, s2, 7
	s_and_b32 s1, s1, 8
	s_lshr_b32 s34, s19, 6
	s_lshr_b32 s55, s19, 6
	s_lshl_b64 s[12:13], s[20:21], 11
	s_xor_b32 s16, s27, 0x700
	s_or_b32 s18, s1, s0
	s_or_b32 s0, s12, s16
	s_lshl_b32 s24, s34, 5
	s_add_u32 s0, s0, s24
	s_addc_u32 s1, s13, 0
	s_lshl_b64 s[14:15], s[0:1], 10
	s_lshl_b64 s[0:1], s[0:1], 11
	s_waitcnt lgkmcnt(0)
	s_add_u32 s0, s4, s0
	s_addc_u32 s1, s5, s1
	s_lshl_b32 s33, s18, 6
	s_lshl_b32 s2, s18, 7
	s_add_u32 s2, s0, s2
	s_addc_u32 s3, s1, 0
	s_lshl_b32 s0, s20, 4
	s_or_b32 s20, s18, s0
	s_and_b32 s17, s19, 0x3fffffc0
	s_lshl_b64 s[0:1], s[20:21], 18
	s_add_u32 s28, s6, s0
	s_addc_u32 s29, s7, s1
	s_lshl_b32 s18, s34, 10
	s_add_u32 s6, s28, s18
	s_addc_u32 s7, s29, 0
	s_add_u32 s30, s8, s0
	s_addc_u32 s31, s9, s1
	s_lshl_b32 s0, s19, 4
	v_and_b32_e32 v207, 63, v0
	s_and_b32 s0, s0, 0xfffff000
	v_mov_b32_e32 v3, 0
	v_lshlrev_b32_e32 v2, 4, v207
	s_add_u32 s0, s30, s0
	v_lshl_add_u64 v[212:213], s[6:7], 0, v[2:3]
	s_addc_u32 s1, s31, 0
	s_lshr_b32 s6, s19, 2
	v_bfe_u32 v1, v0, 2, 4
	v_and_or_b32 v2, s6, 48, v1
	v_lshlrev_b32_e32 v2, 6, v2
	v_lshlrev_b32_e32 v209, 3, v0
	s_cmp_lg_u32 0, -1
	v_lshl_add_u64 v[4:5], s[0:1], 0, v[2:3]
	v_and_b32_e32 v208, 24, v209
	s_cselect_b32 s0, 0, 0
	v_and_b32_e32 v222, 31, v0
	v_lshlrev_b32_e32 v2, 1, v208
	s_add_i32 s35, s18, s0
	s_mov_b32 s0, m0
	s_mov_b32 m0, s35
	s_nop 0
	global_load_lds_dwordx4 v[212:213], off
	s_mov_b32 m0, s0
	v_bfe_u32 v211, v0, 5, 1
	v_lshl_add_u64 v[194:195], v[4:5], 0, v[2:3]
	s_add_i32 s39, s35, 0x6000
	s_mov_b32 s0, m0
	s_mov_b32 m0, s39
	s_nop 0
	global_load_lds_dwordx4 v[194:195], off
	s_mov_b32 m0, s0
	v_lshlrev_b32_e32 v2, 10, v222
	s_mov_b64 s[0:1], 0x2000
	v_lshl_or_b32 v210, v211, 3, v2
	v_lshl_add_u64 v[214:215], v[212:213], 0, s[0:1]
	s_add_i32 s36, s35, 0x2000
	s_mov_b32 s6, m0
	s_mov_b32 m0, s36
	s_nop 0
	global_load_lds_dwordx4 v[214:215], off
	s_mov_b32 m0, s6
	v_lshlrev_b32_e32 v2, 1, v210
	global_load_dwordx4 v[158:161], v2, s[2:3]
	global_load_dwordx4 v[154:157], v2, s[2:3] offset:32
	global_load_dwordx4 v[150:153], v2, s[2:3] offset:64
	global_load_dwordx4 v[146:149], v2, s[2:3] offset:96
	v_lshlrev_b32_e32 v4, 10, v211
	v_lshlrev_b32_e32 v5, 4, v222
	v_add3_u32 v224, 0, v4, v5
	v_mov_b32_e32 v4, v3
	v_mov_b32_e32 v5, v3
	v_mov_b32_e32 v6, v3
	v_mov_b32_e32 v7, v3
	v_mov_b32_e32 v8, v3
	v_mov_b32_e32 v9, v3
	v_mov_b32_e32 v10, v3
	v_mov_b32_e32 v11, v3
	v_mov_b32_e32 v12, v3
	v_mov_b32_e32 v13, v3
	v_mov_b32_e32 v14, v3
	v_mov_b32_e32 v15, v3
	v_mov_b32_e32 v16, v3
	v_mov_b32_e32 v17, v3
	v_mov_b32_e32 v18, v3
	v_mov_b32_e32 v19, v3
	s_mov_b64 s[2:3], 0x4000
	s_add_i32 s37, s35, 0x4000
	v_lshl_add_u64 v[216:217], v[212:213], 0, s[2:3]
	s_mov_b32 s6, m0
	s_mov_b32 m0, s37
	s_nop 0
	global_load_lds_dwordx4 v[216:217], off
	s_mov_b32 m0, s6
	s_waitcnt vmcnt(3) lgkmcnt(0)
	s_barrier
	ds_read_b128 v[36:39], v224
	ds_read_b128 v[40:43], v224 offset:512
	s_mov_b64 s[6:7], 0x6000
	s_mov_b32 s41, 3
	s_movk_i32 s46, 0x2000
	s_movk_i32 s25, 0x4000
	s_sub_i32 s43, 0xbf, s16
	s_mov_b32 s45, 0x41000000
	s_mov_b64 s[18:19], 0xa000
	v_lshlrev_b32_e32 v226, 4, v211
	v_mov_b32_e32 v233, v3
	v_lshlrev_b32_e32 v206, 3, v207
	s_waitcnt vmcnt(3) lgkmcnt(1)
	v_mfma_f32_32x32x16_f16 v[20:35], v[36:39], v[158:161], v[4:19]
	s_waitcnt lgkmcnt(0)
	v_mfma_f32_32x32x16_f16 v[4:19], v[40:43], v[158:161], v[4:19]
	ds_read_b128 v[36:39], v224 offset:2048
	ds_read_b128 v[40:43], v224 offset:2560
	s_waitcnt vmcnt(2) lgkmcnt(1)
	v_mfma_f32_32x32x16_f16 v[20:35], v[36:39], v[154:157], v[20:35]
	s_waitcnt lgkmcnt(0)
	v_mfma_f32_32x32x16_f16 v[4:19], v[40:43], v[154:157], v[4:19]
	ds_read_b128 v[36:39], v224 offset:4096
	ds_read_b128 v[40:43], v224 offset:4608
	s_waitcnt vmcnt(1) lgkmcnt(1)
	v_mfma_f32_32x32x16_f16 v[20:35], v[36:39], v[150:153], v[20:35]
	s_waitcnt lgkmcnt(0)
	v_mfma_f32_32x32x16_f16 v[4:19], v[40:43], v[150:153], v[4:19]
	ds_read_b128 v[36:39], v224 offset:6144
	ds_read_b128 v[40:43], v224 offset:6656
	s_waitcnt vmcnt(0) lgkmcnt(1)
	v_mfma_f32_32x32x16_f16 v[20:35], v[36:39], v[146:149], v[20:35]
	s_waitcnt lgkmcnt(0)
	v_mfma_f32_32x32x16_f16 v[4:19], v[40:43], v[146:149], v[4:19]
	s_nop 15
	s_nop 7
	s_nop 0
	v_max3_f32 v2, v20, v21, v4
	v_max3_f32 v36, v22, v23, v5
	s_nop 0
	v_max3_f32 v2, v2, v6, v7
	v_max3_f32 v36, v36, v26, v27
	s_nop 0
	v_max3_f32 v2, v2, v24, v25
	v_max3_f32 v36, v36, v10, v11
	s_nop 0
	v_max3_f32 v2, v2, v8, v9
	v_max3_f32 v36, v36, v30, v31
	s_nop 0
	v_max3_f32 v2, v2, v28, v29
	v_max3_f32 v36, v36, v14, v15
	s_nop 0
	v_max3_f32 v2, v2, v12, v13
	v_max3_f32 v36, v36, v34, v35
	s_nop 0
	v_max3_f32 v2, v2, v32, v33
	v_max3_f32 v36, v36, v18, v19
	s_nop 0
	v_max3_f32 v2, v2, v16, v17
	s_nop 0
	v_max_f32_e32 v2, v2, v36
	s_nop 0
	v_mov_b32_e32 v36, v2
	s_nop 1
	v_permlane32_swap_b32_e32 v2, v36
	v_max_f32_e32 v2, v2, v36
	s_nop 0
	v_sub_f32_e32 v50, v34, v2
	v_add_f32_e32 v231, v3, v2
	v_sub_f32_e32 v51, v35, v2
	v_sub_f32_e32 v52, v4, v2
	v_sub_f32_e32 v53, v5, v2
	v_lshl_add_u64 v[4:5], v[212:213], 0, s[6:7]
	v_xor_b32_e32 v34, 0x80000000, v231
	v_mov_b32_e32 v35, v34
	v_mov_b32_e32 v36, v34
	v_mov_b32_e32 v37, v34
	v_mov_b32_e32 v38, v34
	v_mov_b32_e32 v39, v34
	v_mov_b32_e32 v40, v34
	v_mov_b32_e32 v41, v34
	v_mov_b32_e32 v42, v34
	v_mov_b32_e32 v43, v34
	v_mov_b32_e32 v44, v34
	v_mov_b32_e32 v45, v34
	v_mov_b32_e32 v46, v34
	v_mov_b32_e32 v47, v34
	v_mov_b32_e32 v48, v34
	v_mov_b32_e32 v49, v34
	s_waitcnt vmcnt(0) lgkmcnt(0)
	s_barrier
	s_mov_b32 s8, m0
	s_mov_b32 m0, s35
	s_nop 0
	global_load_lds_dwordx4 v[4:5], off
	s_mov_b32 m0, s8
	s_add_i32 s8, s35, 0x8000
	v_lshl_add_u64 v[4:5], v[194:195], 0, s[0:1]
	s_mov_b32 s0, m0
	s_mov_b32 m0, s8
	s_nop 0
	global_load_lds_dwordx4 v[4:5], off
	s_mov_b32 m0, s0
	ds_read_b128 v[190:193], v224 offset:8192
	ds_read_b128 v[186:189], v224 offset:8704
	ds_read_b128 v[182:185], v224 offset:10240
	ds_read_b128 v[178:181], v224 offset:10752
	ds_read_b128 v[174:177], v224 offset:12288
	ds_read_b128 v[170:173], v224 offset:12800
	ds_read_b128 v[166:169], v224 offset:14336
	ds_read_b128 v[162:165], v224 offset:14848
	v_sub_f32_e32 v20, v20, v2
	v_sub_f32_e32 v21, v21, v2
	v_sub_f32_e32 v22, v22, v2
	v_sub_f32_e32 v23, v23, v2
	v_sub_f32_e32 v24, v24, v2
	v_sub_f32_e32 v25, v25, v2
	v_sub_f32_e32 v26, v26, v2
	v_sub_f32_e32 v27, v27, v2
	v_sub_f32_e32 v28, v28, v2
	v_sub_f32_e32 v29, v29, v2
	v_sub_f32_e32 v30, v30, v2
	v_sub_f32_e32 v31, v31, v2
	v_sub_f32_e32 v32, v32, v2
	v_sub_f32_e32 v33, v33, v2
	v_sub_f32_e32 v6, v6, v2
	v_sub_f32_e32 v7, v7, v2
	v_sub_f32_e32 v8, v8, v2
	v_sub_f32_e32 v9, v9, v2
	v_sub_f32_e32 v10, v10, v2
	v_sub_f32_e32 v11, v11, v2
	v_sub_f32_e32 v12, v12, v2
	v_sub_f32_e32 v13, v13, v2
	v_sub_f32_e32 v14, v14, v2
	v_sub_f32_e32 v15, v15, v2
	v_sub_f32_e32 v16, v16, v2
	v_sub_f32_e32 v17, v17, v2
	v_sub_f32_e32 v18, v18, v2
	v_sub_f32_e32 v19, v19, v2
	v_lshlrev_b32_e32 v2, 1, v0
	v_and_b32_e32 v228, 32, v2
	v_lshlrev_b32_e32 v2, 4, v0
	v_exp_f32_e32 v81, v51
	v_exp_f32_e32 v66, v20
	v_exp_f32_e32 v67, v21
	v_exp_f32_e32 v68, v22
	v_exp_f32_e32 v69, v23
	v_exp_f32_e32 v70, v24
	v_exp_f32_e32 v71, v25
	v_exp_f32_e32 v72, v26
	v_exp_f32_e32 v73, v27
	v_exp_f32_e32 v74, v28
	v_exp_f32_e32 v75, v29
	v_exp_f32_e32 v76, v30
	v_exp_f32_e32 v77, v31
	v_exp_f32_e32 v78, v32
	v_exp_f32_e32 v79, v33
	v_exp_f32_e32 v80, v50
	v_exp_f32_e32 v65, v19
	v_exp_f32_e32 v50, v52
	v_exp_f32_e32 v51, v53
	v_exp_f32_e32 v52, v6
	v_exp_f32_e32 v53, v7
	v_exp_f32_e32 v54, v8
	v_exp_f32_e32 v55, v9
	v_exp_f32_e32 v56, v10
	v_exp_f32_e32 v57, v11
	v_exp_f32_e32 v58, v12
	v_exp_f32_e32 v59, v13
	v_exp_f32_e32 v60, v14
	v_exp_f32_e32 v61, v15
	v_exp_f32_e32 v62, v16
	v_exp_f32_e32 v63, v17
	v_exp_f32_e32 v64, v18
	v_and_b32_e32 v2, 0xc0, v2
	s_add_i32 s0, s16, 0x100
	v_lshl_or_b32 v230, v211, 8, v2
	v_add_u32_e32 v2, 0, v228
	v_mov_b32_e32 v16, v3
	v_mov_b32_e32 v17, v3
	s_lshr_b32 s42, s0, 6
	s_lshl_b32 s0, s17, 2
	s_waitcnt vmcnt(2) lgkmcnt(0)
	s_barrier
	v_add3_u32 v225, v2, v208, v230
	v_mov_b32_e32 v2, v3
	v_mov_b32_e32 v4, v3
	v_mov_b32_e32 v5, v3
	v_mov_b32_e32 v6, v3
	v_mov_b32_e32 v7, v3
	v_mov_b32_e32 v8, v3
	v_mov_b32_e32 v9, v3
	v_mov_b32_e32 v10, v3
	v_mov_b32_e32 v11, v3
	v_mov_b32_e32 v12, v3
	v_mov_b32_e32 v13, v3
	v_mov_b32_e32 v14, v3
	v_mov_b32_e32 v15, v3
	s_add_i32 s38, s0, 0
	v_mov_b64_e32 v[32:33], v[16:17]
	v_cmp_gt_u32_e64 s[0:1], 32, v207
	s_mov_b64 s[8:9], 0
	s_mov_b64 s[16:17], 0x8000
	v_lshl_add_u32 v223, v222, 2, s38
	v_mov_b64_e32 v[30:31], v[14:15]
	v_mov_b64_e32 v[28:29], v[12:13]
	v_mov_b64_e32 v[26:27], v[10:11]
	v_mov_b64_e32 v[24:25], v[8:9]
	v_mov_b64_e32 v[22:23], v[6:7]
	v_mov_b64_e32 v[20:21], v[4:5]
	v_mov_b64_e32 v[18:19], v[2:3]

.LBB2_88:
	v_add_u32_e32 v114, s44, v225
	ds_read_b64_tr_b16 v[110:111], v114 offset:24576
	ds_read_b64_tr_b16 v[112:113], v114 offset:25088
	v_add_f32_e32 v82, v66, v67
	v_add_f32_e32 v82, v68, v82
	v_add_f32_e32 v82, v69, v82
	v_add_f32_e32 v82, v70, v82
	v_add_f32_e32 v98, v71, v82
	s_waitcnt lgkmcnt(9)
	s_cmp_lt_u32 s55, 6
	s_cbranch_scc1 .Lmsk_7830
	v_mfma_f32_32x32x16_f16 v[82:97], v[190:193], v[158:161], v[34:49]
.Lmsk_7830:
	v_cvt_pk_f16_f32 v142, v66, v67
	v_cvt_pk_f16_f32 v143, v68, v69
	ds_read_b64_tr_b16 v[106:107], v114 offset:28672
	ds_read_b64_tr_b16 v[108:109], v114 offset:29184
	s_waitcnt lgkmcnt(10)
	s_cmp_lt_u32 s55, 7
	s_cbranch_scc1 .Lmsk_7842
	v_mfma_f32_32x32x16_f16 v[34:49], v[186:189], v[158:161], v[34:49]
.Lmsk_7842:
	v_add_f32_e32 v66, v72, v98
	v_add_f32_e32 v66, v73, v66
	v_add_f32_e32 v66, v74, v66
	v_add_f32_e32 v66, v75, v66
	v_cvt_pk_f16_f32 v144, v70, v71
	v_cvt_pk_f16_f32 v145, v72, v73
	ds_read_b64_tr_b16 v[102:103], v114 offset:25600
	ds_read_b64_tr_b16 v[104:105], v114 offset:26112
	s_waitcnt lgkmcnt(11)
	s_cmp_lt_u32 s55, 6
	s_cbranch_scc1 .Lmsk_7858
	v_mfma_f32_32x32x16_f16 v[82:97], v[182:185], v[154:157], v[82:97]
.Lmsk_7858:
	v_add_f32_e32 v66, v76, v66
	v_add_f32_e32 v66, v77, v66
	v_add_f32_e32 v66, v78, v66
	v_add_f32_e32 v66, v79, v66
	v_cvt_pk_f16_f32 v138, v74, v75
	v_cvt_pk_f16_f32 v139, v76, v77
	ds_read_b64_tr_b16 v[98:99], v114 offset:29696
	ds_read_b64_tr_b16 v[100:101], v114 offset:30208
	s_waitcnt lgkmcnt(12)
	s_cmp_lt_u32 s55, 7
	s_cbranch_scc1 .Lmsk_7874
	v_mfma_f32_32x32x16_f16 v[34:49], v[178:181], v[154:157], v[34:49]
.Lmsk_7874:
	v_add_f32_e32 v66, v80, v66
	v_add_f32_e32 v66, v81, v66
	v_add_f32_e32 v66, v50, v66
	v_add_f32_e32 v66, v51, v66
	v_cvt_pk_f16_f32 v140, v78, v79
	v_cvt_pk_f16_f32 v141, v80, v81
	ds_read_b64_tr_b16 v[78:79], v114 offset:26624
	ds_read_b64_tr_b16 v[80:81], v114 offset:27136
	s_waitcnt lgkmcnt(13)
	s_cmp_lt_u32 s55, 6
	s_cbranch_scc1 .Lmsk_7890
	v_mfma_f32_32x32x16_f16 v[82:97], v[174:177], v[150:153], v[82:97]
.Lmsk_7890:
	v_add_f32_e32 v66, v52, v66
	v_add_f32_e32 v66, v53, v66
	v_add_f32_e32 v66, v54, v66
	v_add_f32_e32 v66, v55, v66
	v_cvt_pk_f16_f32 v134, v50, v51
	v_cvt_pk_f16_f32 v135, v52, v53
	ds_read_b64_tr_b16 v[74:75], v114 offset:30720
	ds_read_b64_tr_b16 v[76:77], v114 offset:31232
	s_waitcnt lgkmcnt(14)
	s_cmp_lt_u32 s55, 7
	s_cbranch_scc1 .Lmsk_7906
	v_mfma_f32_32x32x16_f16 v[34:49], v[170:173], v[150:153], v[34:49]
.Lmsk_7906:
	v_add_f32_e32 v50, v56, v66
	v_add_f32_e32 v50, v57, v50
	v_add_f32_e32 v50, v58, v50
	v_add_f32_e32 v50, v59, v50
	v_cvt_pk_f16_f32 v136, v54, v55
	v_cvt_pk_f16_f32 v137, v56, v57
	ds_read_b64_tr_b16 v[70:71], v114 offset:27648
	ds_read_b64_tr_b16 v[72:73], v114 offset:28160
	s_waitcnt lgkmcnt(14)
	s_cmp_lt_u32 s55, 6
	s_cbranch_scc1 .Lmsk_7922
	v_mfma_f32_32x32x16_f16 v[82:97], v[166:169], v[146:149], v[82:97]
.Lmsk_7922:
	v_add_f32_e32 v50, v60, v50
	v_add_f32_e32 v50, v61, v50
	v_add_f32_e32 v50, v62, v50
	v_add_f32_e32 v50, v63, v50
	v_cvt_pk_f16_f32 v130, v58, v59
	v_cvt_pk_f16_f32 v131, v60, v61
	ds_read_b64_tr_b16 v[66:67], v114 offset:31744
	ds_read_b64_tr_b16 v[68:69], v114 offset:32256
	s_cmp_lt_u32 s55, 7
	s_cbranch_scc1 .Lmsk_7937
	v_mfma_f32_32x32x16_f16 v[34:49], v[162:165], v[146:149], v[34:49]
.Lmsk_7937:
	v_add_f32_e32 v50, v64, v50
	v_add_f32_e32 v50, v65, v50
	v_add_f32_e32 v50, 0, v50
	v_cvt_pk_f16_f32 v132, v62, v63
	v_cvt_pk_f16_f32 v133, v64, v65
	v_readfirstlane_b32 s2, v232
	s_and_b32 s6, s2, 0xffffffe0
	s_or_b32 s7, s2, 31
	s_cmpk_lt_i32 s7, 0xc0
	v_or_b32_e32 v229, 0xc0, v227
	s_cbranch_scc1 .LBB2_98
	s_cmpk_gt_i32 s6, 0xde
	s_cbranch_scc1 .LBB2_93
	v_mov_b32_e32 v51, 0xff800000
	v_cmp_lt_u32_e32 vcc, v229, v232
	v_or_b32_e32 v52, 0xc2, v227
	s_mov_b32 s8, 0xff800000
	v_cndmask_b32_e32 v83, v51, v83, vcc
	v_cmp_le_u32_e32 vcc, v229, v232
	s_nop 1
	v_cndmask_b32_e32 v82, v51, v82, vcc
	v_cmp_le_u32_e32 vcc, v52, v232
	v_or_b32_e32 v52, 0xc3, v227
	s_nop 0
	v_cndmask_b32_e32 v84, v51, v84, vcc
	v_cmp_le_u32_e32 vcc, v52, v232
	v_or_b32_e32 v52, 0xc8, v227
	s_nop 0
	v_cndmask_b32_e32 v85, v51, v85, vcc
	v_cmp_le_u32_e32 vcc, v52, v232
	v_or_b32_e32 v52, 0xc9, v227
	s_nop 0
	v_cndmask_b32_e32 v86, v51, v86, vcc
	v_cmp_le_u32_e32 vcc, v52, v232
	v_or_b32_e32 v52, 0xca, v227
	s_nop 0
	v_cndmask_b32_e32 v87, v51, v87, vcc
	v_cmp_le_u32_e32 vcc, v52, v232
	v_or_b32_e32 v52, 0xcb, v227
	s_nop 0
	v_cndmask_b32_e32 v88, v51, v88, vcc
	v_cmp_le_u32_e32 vcc, v52, v232
	v_or_b32_e32 v52, 0xd0, v227
	s_nop 0
	v_cndmask_b32_e32 v89, v51, v89, vcc
	v_cmp_le_u32_e32 vcc, v52, v232
	v_or_b32_e32 v52, 0xd1, v227
	s_nop 0
	v_cndmask_b32_e32 v90, v51, v90, vcc
	v_cmp_le_u32_e32 vcc, v52, v232
	v_or_b32_e32 v52, 0xd2, v227
	s_nop 0
	v_cndmask_b32_e32 v91, v51, v91, vcc
	v_cmp_le_u32_e32 vcc, v52, v232
	v_or_b32_e32 v52, 0xd3, v227
	s_nop 0
	v_cndmask_b32_e32 v92, v51, v92, vcc
	v_cmp_le_u32_e32 vcc, v52, v232
	v_or_b32_e32 v52, 0xd8, v227
	s_nop 0
	v_cndmask_b32_e32 v93, v51, v93, vcc
	v_cmp_le_u32_e32 vcc, v52, v232
	v_or_b32_e32 v52, 0xd9, v227
	s_nop 0
	v_cndmask_b32_e32 v94, v51, v94, vcc
	v_cmp_le_u32_e32 vcc, v52, v232
	v_or_b32_e32 v52, 0xda, v227
	s_nop 0
	v_cndmask_b32_e32 v95, v51, v95, vcc
	v_cmp_le_u32_e32 vcc, v52, v232
	s_nop 1
	v_cndmask_b32_e32 v96, v51, v96, vcc
	v_or_b32_e32 v51, 0xdb, v227
	v_cmp_gt_u32_e32 vcc, v51, v232
	s_and_saveexec_b64 s[2:3], vcc
	v_mov_b32_e32 v97, s8
	s_or_b64 exec, exec, s[2:3]

.LBB2_101:
	s_waitcnt lgkmcnt(14)
	s_cmp_lt_u32 s55, 4
	s_cbranch_scc1 .Lmsk_8170
	v_mfma_f32_32x32x16_f16 v[2:17], v[142:145], v[110:113], v[2:17]
.Lmsk_8170:
	v_exp_f32_e32 v82, v82
	v_exp_f32_e32 v83, v83
	v_exp_f32_e32 v84, v84
	v_exp_f32_e32 v85, v85
	s_waitcnt lgkmcnt(12)
	s_cmp_lt_u32 s55, 4
	s_cbranch_scc1 .Lmsk_8179
	v_mfma_f32_32x32x16_f16 v[18:33], v[142:145], v[106:109], v[18:33]
.Lmsk_8179:
	v_exp_f32_e32 v86, v86
	v_exp_f32_e32 v87, v87
	v_exp_f32_e32 v88, v88
	v_exp_f32_e32 v89, v89
	s_waitcnt lgkmcnt(10)
	s_cmp_lt_u32 s55, 4
	s_cbranch_scc1 .Lmsk_8188
	v_mfma_f32_32x32x16_f16 v[2:17], v[138:141], v[102:105], v[2:17]
.Lmsk_8188:
	v_exp_f32_e32 v90, v90
	v_exp_f32_e32 v91, v91
	v_exp_f32_e32 v92, v92
	v_exp_f32_e32 v93, v93
	s_waitcnt lgkmcnt(8)
	s_cmp_lt_u32 s55, 4
	s_cbranch_scc1 .Lmsk_8197
	v_mfma_f32_32x32x16_f16 v[18:33], v[138:141], v[98:101], v[18:33]
.Lmsk_8197:
	v_exp_f32_e32 v94, v94
	v_exp_f32_e32 v95, v95
	v_exp_f32_e32 v96, v96
	v_exp_f32_e32 v97, v97
	s_waitcnt lgkmcnt(6)
	s_cmp_lt_u32 s55, 5
	s_cbranch_scc1 .Lmsk_8206
	v_mfma_f32_32x32x16_f16 v[2:17], v[134:137], v[78:81], v[2:17]
.Lmsk_8206:
	v_exp_f32_e32 v34, v34
	v_exp_f32_e32 v35, v35
	v_exp_f32_e32 v36, v36
	v_exp_f32_e32 v37, v37
	s_waitcnt lgkmcnt(4)
	s_cmp_lt_u32 s55, 5
	s_cbranch_scc1 .Lmsk_8215
	v_mfma_f32_32x32x16_f16 v[18:33], v[134:137], v[74:77], v[18:33]
.Lmsk_8215:
	v_exp_f32_e32 v38, v38
	v_exp_f32_e32 v39, v39
	v_exp_f32_e32 v40, v40
	v_exp_f32_e32 v41, v41
	s_waitcnt lgkmcnt(2)
	s_cmp_lt_u32 s55, 5
	s_cbranch_scc1 .Lmsk_8224
	v_mfma_f32_32x32x16_f16 v[2:17], v[130:133], v[70:73], v[2:17]
.Lmsk_8224:
	v_exp_f32_e32 v42, v42
	v_exp_f32_e32 v43, v43
	v_exp_f32_e32 v44, v44
	v_exp_f32_e32 v45, v45
	s_waitcnt lgkmcnt(0)
	s_cmp_lt_u32 s55, 5
	s_cbranch_scc1 .Lmsk_8233
	v_mfma_f32_32x32x16_f16 v[18:33], v[130:133], v[66:69], v[18:33]
.Lmsk_8233:
	v_exp_f32_e32 v46, v46
	v_exp_f32_e32 v47, v47
	v_exp_f32_e32 v48, v48
	v_exp_f32_e32 v49, v49
	s_andn2_b64 vcc, exec, s[2:3]
	v_lshl_add_u32 v50, v227, 2, s38
	s_cbranch_vccnz .LBB2_103
	s_waitcnt lgkmcnt(0)
	ds_read_b128 v[52:55], v50 offset:49248
	ds_read_b128 v[56:59], v50 offset:49216
	ds_read_b128 v[60:63], v50 offset:49184
	ds_read_b128 v[64:67], v50 offset:49152
	s_waitcnt lgkmcnt(3)
	v_pk_mul_f32 v[16:17], v[16:17], v[54:55]
	s_waitcnt lgkmcnt(2)
	v_pk_mul_f32 v[12:13], v[12:13], v[58:59]
	s_waitcnt lgkmcnt(1)
	v_pk_mul_f32 v[8:9], v[8:9], v[62:63]
	s_waitcnt lgkmcnt(0)
	v_pk_mul_f32 v[4:5], v[4:5], v[66:67]
	v_pk_mul_f32 v[14:15], v[14:15], v[52:53]
	v_pk_mul_f32 v[10:11], v[10:11], v[56:57]
	v_pk_mul_f32 v[6:7], v[6:7], v[60:61]
	v_pk_mul_f32 v[2:3], v[2:3], v[64:65]
	v_pk_mul_f32 v[32:33], v[32:33], v[54:55]
	v_pk_mul_f32 v[28:29], v[28:29], v[58:59]
	v_pk_mul_f32 v[24:25], v[24:25], v[62:63]
	v_pk_mul_f32 v[20:21], v[20:21], v[66:67]
	v_pk_mul_f32 v[30:31], v[30:31], v[52:53]
	v_pk_mul_f32 v[26:27], v[26:27], v[56:57]
	v_pk_mul_f32 v[22:23], v[22:23], v[60:61]
	v_pk_mul_f32 v[18:19], v[18:19], v[64:65]
.LBB2_103:
	s_cmp_lg_u32 0, -1
	s_cselect_b32 s2, 0, 0
	s_addk_i32 s2, 0x6000
	v_add_u32_e32 v51, s2, v228
	v_add3_u32 v228, v51, v208, v230
	v_add_f32_e32 v51, v82, v83
	v_add_f32_e32 v51, v84, v51
	v_add_f32_e32 v51, v85, v51
	v_add_f32_e32 v51, v86, v51
	v_add_f32_e32 v51, v87, v51
	v_add_f32_e32 v51, v88, v51
	v_add_f32_e32 v51, v89, v51
	v_add_f32_e32 v51, v90, v51
	v_add_f32_e32 v51, v91, v51
	v_add_f32_e32 v51, v92, v51
	v_add_f32_e32 v51, v93, v51
	v_add_f32_e32 v51, v94, v51
	v_add_f32_e32 v51, v95, v51
	v_add_f32_e32 v51, v96, v51
	v_add_f32_e32 v51, v97, v51
	v_add_f32_e32 v51, v34, v51
	v_add_f32_e32 v51, v35, v51
	v_add_f32_e32 v51, v36, v51
	v_add_f32_e32 v51, v37, v51
	v_add_f32_e32 v51, v38, v51
	v_add_f32_e32 v51, v39, v51
	v_add_f32_e32 v51, v40, v51
	v_add_f32_e32 v51, v41, v51
	v_add_f32_e32 v51, v42, v51
	v_add_f32_e32 v51, v43, v51
	v_add_f32_e32 v51, v44, v51
	v_add_f32_e32 v51, v45, v51
	s_mov_b32 s2, m0
	s_mov_b32 m0, s35
	s_nop 0
	global_load_lds_dwordx4 v[212:213], off
	s_mov_b32 m0, s2
	v_add_f32_e32 v51, v46, v51
	s_mov_b32 s2, m0
	s_mov_b32 m0, s36
	s_nop 0
	global_load_lds_dwordx4 v[214:215], off
	s_mov_b32 m0, s2
	v_add_f32_e32 v51, v47, v51
	s_mov_b32 s2, m0
	s_mov_b32 m0, s37
	s_nop 0
	global_load_lds_dwordx4 v[216:217], off
	s_mov_b32 m0, s2
	v_add_f32_e32 v51, v48, v51
	v_add_f32_e32 v51, v49, v51
	v_add_f32_e32 v51, v114, v51
	v_cvt_pk_f16_f32 v34, v34, v35
	v_cvt_pk_f16_f32 v52, v82, v83
	v_cvt_pk_f16_f32 v53, v84, v85
	v_cvt_pk_f16_f32 v54, v86, v87
	v_cvt_pk_f16_f32 v55, v88, v89
	v_cvt_pk_f16_f32 v56, v90, v91
	v_cvt_pk_f16_f32 v57, v92, v93
	v_cvt_pk_f16_f32 v58, v94, v95
	v_cvt_pk_f16_f32 v59, v96, v97
	v_cvt_pk_f16_f32 v35, v36, v37
	v_cvt_pk_f16_f32 v36, v38, v39
	v_cvt_pk_f16_f32 v37, v40, v41
	v_cvt_pk_f16_f32 v38, v42, v43
	v_cvt_pk_f16_f32 v39, v44, v45
	v_cvt_pk_f16_f32 v40, v46, v47
	v_cvt_pk_f16_f32 v41, v48, v49
	v_add_u32_e32 v72, s40, v228
	ds_read_b64_tr_b16 v[42:43],v72 offset:0
	ds_read_b64_tr_b16 v[44:45],v72 offset:512
	ds_read_b64_tr_b16 v[46:47],v72 offset:1024
	ds_read_b64_tr_b16 v[48:49],v72 offset:1536
	ds_read_b64_tr_b16 v[60:61],v72 offset:2048
	ds_read_b64_tr_b16 v[62:63],v72 offset:2560
	ds_read_b64_tr_b16 v[64:65],v72 offset:3072
	ds_read_b64_tr_b16 v[66:67],v72 offset:3584
	s_waitcnt lgkmcnt(0)
	s_nop 0
	s_cmp_lt_u32 s55, 6
	s_cbranch_scc1 .Lmsk_8378
	v_mfma_f32_32x32x16_f16 v[2:17], v[52:55], v[42:45], v[2:17]
.Lmsk_8378:
	ds_read_b64_tr_b16 v[42:43],v72 offset:4096
	ds_read_b64_tr_b16 v[44:45],v72 offset:4608
	s_cmp_lt_u32 s55, 6
	s_cbranch_scc1 .Lmsk_8385
	v_mfma_f32_32x32x16_f16 v[2:17], v[56:59], v[46:49], v[2:17]
.Lmsk_8385:
	ds_read_b64_tr_b16 v[46:47],v72 offset:5120
	ds_read_b64_tr_b16 v[48:49],v72 offset:5632
	s_cmp_lt_u32 s55, 7
	s_cbranch_scc1 .Lmsk_8392
	v_mfma_f32_32x32x16_f16 v[2:17], v[34:37], v[60:63], v[2:17]
.Lmsk_8392:
	ds_read_b64_tr_b16 v[60:61],v72 offset:6144
	ds_read_b64_tr_b16 v[62:63],v72 offset:6656
	ds_read_b64_tr_b16 v[68:69],v72 offset:7168
	ds_read_b64_tr_b16 v[70:71],v72 offset:7680
	s_waitcnt lgkmcnt(0)
	s_cmp_lt_u32 s55, 7
	s_cbranch_scc1 .Lmsk_8408
	v_mfma_f32_32x32x16_f16 v[2:17], v[38:41], v[64:67], v[2:17]
.Lmsk_8408:
	s_cmp_lt_u32 s55, 6
	s_cbranch_scc1 .Lmsk_8410
	v_mfma_f32_32x32x16_f16 v[18:33], v[52:55], v[42:45], v[18:33]
.Lmsk_8410:
	s_cmp_lt_u32 s55, 6
	s_cbranch_scc1 .Lmsk_8411
	v_mfma_f32_32x32x16_f16 v[18:33], v[56:59], v[46:49], v[18:33]
.Lmsk_8411:
	s_cmp_lt_u32 s55, 7
	s_cbranch_scc1 .Lmsk_8412
	v_mfma_f32_32x32x16_f16 v[18:33], v[34:37], v[60:63], v[18:33]
.Lmsk_8412:
	v_mov_b32_e32 v34, v51
	s_nop 1
	v_permlane32_swap_b32_e32 v51, v34
	s_cmp_lt_u32 s55, 7
	s_cbranch_scc1 .Lmsk_8416
	v_mfma_f32_32x32x16_f16 v[18:33], v[38:41], v[68:71], v[18:33]
.Lmsk_8416:
	s_and_saveexec_b64 s[2:3], s[0:1]
	v_add_f32_e32 v34, v51, v34
	ds_write_b32 v223, v34 offset:49280
	s_or_b64 exec, exec, s[2:3]
	s_waitcnt lgkmcnt(0)
	ds_read_b128 v[34:37], v50 offset:49280
	ds_read_b128 v[38:41], v50 offset:49312
	s_lshl_b64 s[2:3], s[14:15], 1
	s_add_u32 s2, s10, s2
	s_addc_u32 s3, s11, s3
	s_waitcnt lgkmcnt(1)
	v_rcp_f32_e32 v42, v34
	v_rcp_f32_e32 v43, v35
	s_lshl_b32 s6, s34, 12
	s_add_i32 s6, s6, 0
	v_lshlrev_b32_e32 v230, 1, v222
	v_lshlrev_b32_e32 v231, 9, v211
	v_rcp_f32_e32 v44, v36
	v_rcp_f32_e32 v45, v37
	s_waitcnt lgkmcnt(0)
	v_rcp_f32_e32 v46, v38
	ds_read_b128 v[34:37], v50 offset:49344
	v_rcp_f32_e32 v47, v39
	v_rcp_f32_e32 v48, v40
	v_rcp_f32_e32 v49, v41
	ds_read_b128 v[38:41], v50 offset:49376
	v_add3_u32 v50, s6, v230, v231
	v_fma_mixlo_f16 v2, v2, v42, 0
	ds_write_b16 v50, v2 offset:51200
	v_fma_mixlo_f16 v2, v18, v42, 0
	ds_write_b16 v50, v2 offset:51264
	v_fma_mixlo_f16 v2, v3, v43, 0
	ds_write_b16 v50, v2 offset:51328
	v_fma_mixlo_f16 v2, v19, v43, 0
	ds_write_b16 v50, v2 offset:51392
	v_fma_mixlo_f16 v2, v4, v44, 0
	ds_write_b16 v50, v2 offset:51456
	v_fma_mixlo_f16 v2, v20, v44, 0
	ds_write_b16 v50, v2 offset:51520
	v_fma_mixlo_f16 v2, v5, v45, 0
	ds_write_b16 v50, v2 offset:51584
	v_fma_mixlo_f16 v2, v21, v45, 0
	ds_write_b16 v50, v2 offset:51648
	v_fma_mixlo_f16 v2, v6, v46, 0
	ds_write_b16 v50, v2 offset:52224
	v_fma_mixlo_f16 v2, v22, v46, 0
	ds_write_b16 v50, v2 offset:52288
	v_fma_mixlo_f16 v2, v7, v47, 0
	ds_write_b16 v50, v2 offset:52352
	v_fma_mixlo_f16 v2, v23, v47, 0
	s_waitcnt lgkmcnt(12)
	v_rcp_f32_e32 v34, v34
	ds_write_b16 v50, v2 offset:52416
	v_fma_mixlo_f16 v2, v8, v48, 0
	ds_write_b16 v50, v2 offset:52480
	v_fma_mixlo_f16 v2, v24, v48, 0
	v_rcp_f32_e32 v35, v35
	ds_write_b16 v50, v2 offset:52544
	v_fma_mixlo_f16 v2, v9, v49, 0
	ds_write_b16 v50, v2 offset:52608
	v_fma_mixlo_f16 v2, v25, v49, 0
	v_rcp_f32_e32 v36, v36
	ds_write_b16 v50, v2 offset:52672
	v_fma_mixlo_f16 v2, v10, v34, 0
	ds_write_b16 v50, v2 offset:53248
	v_fma_mixlo_f16 v2, v26, v34, 0
	v_rcp_f32_e32 v37, v37
	ds_write_b16 v50, v2 offset:53312
	v_fma_mixlo_f16 v2, v11, v35, 0
	ds_write_b16 v50, v2 offset:53376
	v_fma_mixlo_f16 v2, v27, v35, 0
	s_waitcnt lgkmcnt(14)
	v_rcp_f32_e32 v38, v38
	ds_write_b16 v50, v2 offset:53440
	v_fma_mixlo_f16 v2, v12, v36, 0
	ds_write_b16 v50, v2 offset:53504
	v_fma_mixlo_f16 v2, v28, v36, 0
	v_rcp_f32_e32 v39, v39
	ds_write_b16 v50, v2 offset:53568
	v_fma_mixlo_f16 v2, v13, v37, 0
	ds_write_b16 v50, v2 offset:53632
	v_fma_mixlo_f16 v2, v29, v37, 0
	v_rcp_f32_e32 v40, v40
	ds_write_b16 v50, v2 offset:53696
	v_fma_mixlo_f16 v2, v14, v38, 0
	ds_write_b16 v50, v2 offset:54272
	v_fma_mixlo_f16 v2, v30, v38, 0
	v_rcp_f32_e32 v41, v41
	ds_write_b16 v50, v2 offset:54336
	v_fma_mixlo_f16 v2, v15, v39, 0
	ds_write_b16 v50, v2 offset:54400
	v_fma_mixlo_f16 v2, v31, v39, 0
	ds_write_b16 v50, v2 offset:54464
	v_fma_mixlo_f16 v2, v16, v40, 0
	ds_write_b16 v50, v2 offset:54528
	v_fma_mixlo_f16 v2, v32, v40, 0
	ds_write_b16 v50, v2 offset:54592
	v_fma_mixlo_f16 v2, v17, v41, 0
	ds_write_b16 v50, v2 offset:54656
	v_fma_mixlo_f16 v2, v33, v41, 0
	ds_write_b16 v50, v2 offset:54720
	v_and_b32_e32 v2, 56, v209
	s_lshl_b32 s22, s33, 1
	v_lshrrev_b32_e32 v36, 3, v207
	v_lshlrev_b32_e32 v220, 1, v2
	s_add_u32 s2, s2, s22
	v_add_u32_e32 v14, s6, v220
	v_lshlrev_b32_e32 v232, 7, v36
	s_addc_u32 s3, s3, 0
	s_waitcnt lgkmcnt(0)
	v_mov_b32_e32 v221, 0
	v_add_u32_e32 v2, v14, v232
	v_or_b32_e32 v37, 8, v36
	v_lshl_add_u64 v[10:11], s[2:3], 0, v[220:221]
	ds_read_b128 v[2:5], v2 offset:51200
	v_lshlrev_b32_e32 v6, 11, v36
	v_mov_b32_e32 v7, v221
	v_lshlrev_b32_e32 v233, 7, v37
	v_readfirstlane_b32 s8, v0
	v_lshl_add_u64 v[12:13], v[10:11], 0, v[6:7]
	v_add_u32_e32 v6, v14, v233
	s_lshr_b32 s23, s8, 6
	ds_read_b128 v[6:9], v6 offset:51200
	s_or_b32 s2, s12, s27
	s_lshl_b32 s12, s23, 5
	s_add_u32 s6, s2, s12
	s_addc_u32 s7, s13, 0
	s_waitcnt lgkmcnt(1)
	global_store_dwordx4 v[12:13], v[2:5], off sc1
	v_or_b32_e32 v38, 16, v36
	s_lshl_b64 s[2:3], s[6:7], 11
	v_lshlrev_b32_e32 v2, 11, v37
	v_mov_b32_e32 v3, v221
	v_lshl_add_u64 v[2:3], v[10:11], 0, v[2:3]
	v_lshlrev_b32_e32 v234, 7, v38
	s_add_u32 s2, s4, s2
	s_waitcnt lgkmcnt(0)
	global_store_dwordx4 v[2:3], v[6:9], off sc1
	v_add_u32_e32 v2, v14, v234
	v_or_b32_e32 v39, 24, v36
	s_addc_u32 s3, s5, s3
	ds_read_b128 v[2:5], v2 offset:51200
	v_lshlrev_b32_e32 v6, 11, v38
	v_mov_b32_e32 v7, v221
	v_lshlrev_b32_e32 v235, 7, v39
	s_add_u32 s2, s2, s22
	v_lshl_add_u64 v[12:13], v[10:11], 0, v[6:7]
	v_add_u32_e32 v6, v14, v235
	s_addc_u32 s3, s3, 0
	s_lshl_b32 s4, s8, 4
	ds_read_b128 v[6:9], v6 offset:51200
	s_and_b32 s4, s4, 0xfffff000
	s_add_u32 s4, s30, s4
	s_addc_u32 s5, s31, 0
	s_lshr_b32 s9, s8, 2
	s_waitcnt lgkmcnt(1)
	global_store_dwordx4 v[12:13], v[2:5], off sc1
	v_and_or_b32 v0, s9, 48, v1
	s_lshl_b32 s9, s23, 10
	v_lshlrev_b32_e32 v2, 11, v39
	v_mov_b32_e32 v3, v221
	v_lshl_add_u64 v[2:3], v[10:11], 0, v[2:3]
	v_lshlrev_b32_e32 v0, 6, v0
	v_mov_b32_e32 v1, v221
	s_cmp_lg_u32 0, -1
	s_waitcnt lgkmcnt(0)
	global_store_dwordx4 v[2:3], v[6:9], off sc1
	v_lshl_add_u64 v[0:1], s[4:5], 0, v[0:1]
	s_cselect_b32 s4, 0, 0
	s_waitcnt lgkmcnt(0)
	s_barrier
	v_lshlrev_b32_e32 v2, 1, v208
	v_mov_b32_e32 v3, v221
	s_add_i32 s25, s4, s9
	v_lshl_add_u64 v[208:209], v[0:1], 0, v[2:3]
	s_addk_i32 s25, 0x6000
	s_mov_b32 s4, m0
	s_mov_b32 m0, s25
	s_nop 0
	global_load_lds_dwordx4 v[208:209], off
	s_mov_b32 m0, s4
	v_lshlrev_b32_e32 v0, 1, v210
	global_load_dwordx4 v[156:159], v0, s[2:3]
	global_load_dwordx4 v[152:155], v0, s[2:3] offset:32
	global_load_dwordx4 v[148:151], v0, s[2:3] offset:64
	global_load_dwordx4 v[144:147], v0, s[2:3] offset:96
	v_mov_b32_e32 v0, v221
	v_mov_b32_e32 v1, v221
	v_mov_b32_e32 v2, v221
	v_mov_b32_e32 v4, v221
	v_mov_b32_e32 v5, v221
	v_mov_b32_e32 v6, v221
	v_mov_b32_e32 v7, v221
	v_mov_b32_e32 v8, v221
	v_mov_b32_e32 v9, v221
	v_mov_b32_e32 v10, v221
	v_mov_b32_e32 v11, v221
	v_mov_b32_e32 v12, v221
	v_mov_b32_e32 v13, v221
	v_mov_b32_e32 v14, v221
	v_mov_b32_e32 v15, v221
	s_waitcnt vmcnt(5) lgkmcnt(0)
	s_barrier
	ds_read_b128 v[32:35], v224
	s_cmp_lg_u32 s26, 0
	s_waitcnt vmcnt(3) lgkmcnt(0)
	v_mfma_f32_32x32x16_f16 v[16:31], v[32:35], v[156:159], v[0:15]
	ds_read_b128 v[32:35], v224 offset:512
	s_cselect_b64 s[2:3], -1, 0
	v_lshlrev_b32_e32 v239, 10, v36
	v_lshlrev_b32_e32 v238, 10, v37
	v_lshlrev_b32_e32 v237, 10, v38
	v_lshlrev_b32_e32 v236, 10, v39
	v_or_b32_e32 v221, s12, v222
	s_waitcnt lgkmcnt(0)
	v_mfma_f32_32x32x16_f16 v[0:15], v[32:35], v[156:159], v[0:15]
	ds_read_b128 v[32:35], v224 offset:2048
	s_and_b64 vcc, exec, s[2:3]
	s_waitcnt vmcnt(2) lgkmcnt(0)
	v_mfma_f32_32x32x16_f16 v[16:31], v[32:35], v[152:155], v[16:31]
	ds_read_b128 v[32:35], v224 offset:2560
	s_waitcnt lgkmcnt(0)
	v_mfma_f32_32x32x16_f16 v[0:15], v[32:35], v[152:155], v[0:15]
	ds_read_b128 v[32:35], v224 offset:4096
	s_waitcnt vmcnt(1) lgkmcnt(0)
	v_mfma_f32_32x32x16_f16 v[16:31], v[32:35], v[148:151], v[16:31]
	ds_read_b128 v[32:35], v224 offset:4608
	s_waitcnt lgkmcnt(0)
	v_mfma_f32_32x32x16_f16 v[0:15], v[32:35], v[148:151], v[0:15]
	ds_read_b128 v[32:35], v224 offset:6144
	s_waitcnt vmcnt(0) lgkmcnt(0)
	v_mfma_f32_32x32x16_f16 v[16:31], v[32:35], v[144:147], v[16:31]
	ds_read_b128 v[32:35], v224 offset:6656
	s_waitcnt lgkmcnt(0)
	v_mfma_f32_32x32x16_f16 v[0:15], v[32:35], v[144:147], v[0:15]
	s_nop 15
	s_nop 7
	s_cbranch_vccnz .LBB2_119
	v_readfirstlane_b32 s12, v221
	s_cmp_lt_i32 s12, 0
	s_cbranch_scc1 .LBB2_111
	s_cmp_gt_u32 s12, 31
	s_cbranch_scc1 .LBB2_112
	v_mov_b32_e32 v32, 0xff800000
	v_cmp_lt_u32_e32 vcc, v227, v221
	v_or_b32_e32 v33, 2, v227
	s_mov_b32 s13, 0xff800000
	v_cndmask_b32_e32 v17, v32, v17, vcc
	v_cmp_le_u32_e32 vcc, v227, v221
	s_nop 1
	v_cndmask_b32_e32 v16, v32, v16, vcc
	v_cmp_le_u32_e32 vcc, v33, v221
	v_or_b32_e32 v33, 3, v227
	s_nop 0
	v_cndmask_b32_e32 v18, v32, v18, vcc
	v_cmp_le_u32_e32 vcc, v33, v221
	v_or_b32_e32 v33, 8, v227
	s_nop 0
	v_cndmask_b32_e32 v19, v32, v19, vcc
	v_cmp_le_u32_e32 vcc, v33, v221
	v_or_b32_e32 v33, 9, v227
	s_nop 0
	v_cndmask_b32_e32 v20, v32, v20, vcc
	v_cmp_le_u32_e32 vcc, v33, v221
	v_or_b32_e32 v33, 10, v227
	s_nop 0
	v_cndmask_b32_e32 v21, v32, v21, vcc
	v_cmp_le_u32_e32 vcc, v33, v221
	v_or_b32_e32 v33, 11, v227
	s_nop 0
	v_cndmask_b32_e32 v22, v32, v22, vcc
	v_cmp_le_u32_e32 vcc, v33, v221
	v_or_b32_e32 v33, 16, v227
	s_nop 0
	v_cndmask_b32_e32 v23, v32, v23, vcc
	v_cmp_le_u32_e32 vcc, v33, v221
	v_or_b32_e32 v33, 17, v227
	s_nop 0
	v_cndmask_b32_e32 v24, v32, v24, vcc
	v_cmp_le_u32_e32 vcc, v33, v221
	v_or_b32_e32 v33, 18, v227
	s_nop 0
	v_cndmask_b32_e32 v25, v32, v25, vcc
	v_cmp_le_u32_e32 vcc, v33, v221
	v_or_b32_e32 v33, 19, v227
	s_nop 0
	v_cndmask_b32_e32 v26, v32, v26, vcc
	v_cmp_le_u32_e32 vcc, v33, v221
	v_or_b32_e32 v33, 24, v227
	s_nop 0
	v_cndmask_b32_e32 v27, v32, v27, vcc
	v_cmp_le_u32_e32 vcc, v33, v221
	v_or_b32_e32 v33, 25, v227
	s_nop 0
	v_cndmask_b32_e32 v28, v32, v28, vcc
	v_cmp_le_u32_e32 vcc, v33, v221
	v_or_b32_e32 v33, 26, v227
	s_nop 0
	v_cndmask_b32_e32 v29, v32, v29, vcc
	v_cmp_le_u32_e32 vcc, v33, v221
	s_nop 1
	v_cndmask_b32_e32 v30, v32, v30, vcc
	v_or_b32_e32 v32, 27, v227
	v_cmp_gt_u32_e32 vcc, v32, v221
	s_and_saveexec_b64 s[4:5], vcc
	v_mov_b32_e32 v31, s13
	s_or_b64 exec, exec, s[4:5]
	s_branch .LBB2_112

.LBB2_137:
	v_add_u32_e32 v48, s31, v225
	ds_read_b64_tr_b16 v[120:121], v48 offset:24576
	ds_read_b64_tr_b16 v[122:123], v48 offset:25088
	s_waitcnt lgkmcnt(9)
	s_cmp_lt_u32 s55, 6
	s_cbranch_scc1 .Lmsk_9980
	v_mfma_f32_32x32x16_f16 v[96:111], v[204:207], v[156:159], v[32:47]
.Lmsk_9980:
	v_add_f32_e32 v50, v80, v81
	v_add_f32_e32 v50, v82, v50
	v_add_f32_e32 v50, v83, v50
	v_add_f32_e32 v50, v84, v50
	v_add_f32_e32 v50, v85, v50
	v_cvt_pk_f16_f32 v172, v80, v81
	v_cvt_pk_f16_f32 v173, v82, v83
	ds_read_b64_tr_b16 v[116:117], v48 offset:28672
	ds_read_b64_tr_b16 v[118:119], v48 offset:29184
	s_waitcnt lgkmcnt(10)
	s_cmp_lt_u32 s55, 7
	s_cbranch_scc1 .Lmsk_9997
	v_mfma_f32_32x32x16_f16 v[32:47], v[200:203], v[156:159], v[32:47]
.Lmsk_9997:
	v_add_f32_e32 v50, v86, v50
	v_add_f32_e32 v50, v87, v50
	v_add_f32_e32 v50, v88, v50
	v_add_f32_e32 v50, v89, v50
	v_cvt_pk_f16_f32 v174, v84, v85
	v_cvt_pk_f16_f32 v175, v86, v87
	ds_read_b64_tr_b16 v[112:113], v48 offset:25600
	ds_read_b64_tr_b16 v[114:115], v48 offset:26112
	s_waitcnt lgkmcnt(11)
	s_cmp_lt_u32 s55, 6
	s_cbranch_scc1 .Lmsk_10013
	v_mfma_f32_32x32x16_f16 v[96:111], v[196:199], v[152:155], v[96:111]
.Lmsk_10013:
	v_add_f32_e32 v50, v90, v50
	v_add_f32_e32 v50, v91, v50
	v_add_f32_e32 v50, v92, v50
	v_add_f32_e32 v50, v93, v50
	v_cvt_pk_f16_f32 v168, v88, v89
	v_cvt_pk_f16_f32 v169, v90, v91
	ds_read_b64_tr_b16 v[88:89], v48 offset:29696
	ds_read_b64_tr_b16 v[90:91], v48 offset:30208
	s_waitcnt lgkmcnt(12)
	s_cmp_lt_u32 s55, 7
	s_cbranch_scc1 .Lmsk_10029
	v_mfma_f32_32x32x16_f16 v[32:47], v[192:195], v[152:155], v[32:47]
.Lmsk_10029:
	v_add_f32_e32 v50, v94, v50
	v_add_f32_e32 v50, v95, v50
	v_add_f32_e32 v50, v64, v50
	v_add_f32_e32 v50, v65, v50
	v_cvt_pk_f16_f32 v170, v92, v93
	v_cvt_pk_f16_f32 v171, v94, v95
	ds_read_b64_tr_b16 v[84:85], v48 offset:26624
	ds_read_b64_tr_b16 v[86:87], v48 offset:27136
	s_waitcnt lgkmcnt(13)
	s_cmp_lt_u32 s55, 6
	s_cbranch_scc1 .Lmsk_10045
	v_mfma_f32_32x32x16_f16 v[96:111], v[188:191], v[148:151], v[96:111]
.Lmsk_10045:
	v_add_f32_e32 v50, v66, v50
	v_add_f32_e32 v50, v67, v50
	v_add_f32_e32 v50, v68, v50
	v_add_f32_e32 v50, v69, v50
	v_cvt_pk_f16_f32 v164, v64, v65
	v_cvt_pk_f16_f32 v165, v66, v67
	ds_read_b64_tr_b16 v[80:81], v48 offset:30720
	ds_read_b64_tr_b16 v[82:83], v48 offset:31232
	s_waitcnt lgkmcnt(14)
	s_cmp_lt_u32 s55, 7
	s_cbranch_scc1 .Lmsk_10061
	v_mfma_f32_32x32x16_f16 v[32:47], v[184:187], v[148:151], v[32:47]
.Lmsk_10061:
	v_add_f32_e32 v50, v70, v50
	v_add_f32_e32 v50, v71, v50
	v_add_f32_e32 v50, v72, v50
	v_add_f32_e32 v50, v73, v50
	v_cvt_pk_f16_f32 v166, v68, v69
	v_cvt_pk_f16_f32 v167, v70, v71
	ds_read_b64_tr_b16 v[68:69], v48 offset:27648
	ds_read_b64_tr_b16 v[70:71], v48 offset:28160
	s_waitcnt lgkmcnt(14)
	s_cmp_lt_u32 s55, 6
	s_cbranch_scc1 .Lmsk_10077
	v_mfma_f32_32x32x16_f16 v[96:111], v[180:183], v[144:147], v[96:111]
.Lmsk_10077:
	v_add_f32_e32 v50, v74, v50
	v_add_f32_e32 v50, v75, v50
	v_add_f32_e32 v50, v76, v50
	v_add_f32_e32 v50, v77, v50
	v_cvt_pk_f16_f32 v160, v72, v73
	v_cvt_pk_f16_f32 v161, v74, v75
	ds_read_b64_tr_b16 v[64:65], v48 offset:31744
	ds_read_b64_tr_b16 v[66:67], v48 offset:32256
	s_cmp_lt_u32 s55, 7
	s_cbranch_scc1 .Lmsk_10092
	v_mfma_f32_32x32x16_f16 v[32:47], v[176:179], v[144:147], v[32:47]
.Lmsk_10092:
	v_add_f32_e32 v48, v78, v50
	v_add_f32_e32 v48, v79, v48
	v_add_f32_e32 v48, 0, v48
	v_cvt_pk_f16_f32 v162, v76, v77
	v_cvt_pk_f16_f32 v163, v78, v79
	v_readfirstlane_b32 s2, v221
	s_and_b32 s6, s2, 0xffffffe0
	s_or_b32 s7, s2, 31
	s_cmpk_lt_i32 s7, 0xc0
	s_cbranch_scc1 .LBB2_219
	s_cmpk_gt_i32 s6, 0xde
	s_cbranch_scc1 .LBB2_142
	v_mov_b32_e32 v50, 0xff800000
	v_cmp_lt_u32_e32 vcc, v229, v221
	v_or_b32_e32 v51, 0xc2, v227
	s_mov_b32 s8, 0xff800000
	v_cndmask_b32_e32 v97, v50, v97, vcc
	v_cmp_le_u32_e32 vcc, v229, v221
	s_nop 1
	v_cndmask_b32_e32 v96, v50, v96, vcc
	v_cmp_le_u32_e32 vcc, v51, v221
	v_or_b32_e32 v51, 0xc3, v227
	s_nop 0
	v_cndmask_b32_e32 v98, v50, v98, vcc
	v_cmp_le_u32_e32 vcc, v51, v221
	v_or_b32_e32 v51, 0xc8, v227
	s_nop 0
	v_cndmask_b32_e32 v99, v50, v99, vcc
	v_cmp_le_u32_e32 vcc, v51, v221
	v_or_b32_e32 v51, 0xc9, v227
	s_nop 0
	v_cndmask_b32_e32 v100, v50, v100, vcc
	v_cmp_le_u32_e32 vcc, v51, v221
	v_or_b32_e32 v51, 0xca, v227
	s_nop 0
	v_cndmask_b32_e32 v101, v50, v101, vcc
	v_cmp_le_u32_e32 vcc, v51, v221
	v_or_b32_e32 v51, 0xcb, v227
	s_nop 0
	v_cndmask_b32_e32 v102, v50, v102, vcc
	v_cmp_le_u32_e32 vcc, v51, v221
	v_or_b32_e32 v51, 0xd0, v227
	s_nop 0
	v_cndmask_b32_e32 v103, v50, v103, vcc
	v_cmp_le_u32_e32 vcc, v51, v221
	v_or_b32_e32 v51, 0xd1, v227
	s_nop 0
	v_cndmask_b32_e32 v104, v50, v104, vcc
	v_cmp_le_u32_e32 vcc, v51, v221
	v_or_b32_e32 v51, 0xd2, v227
	s_nop 0
	v_cndmask_b32_e32 v105, v50, v105, vcc
	v_cmp_le_u32_e32 vcc, v51, v221
	v_or_b32_e32 v51, 0xd3, v227
	s_nop 0
	v_cndmask_b32_e32 v106, v50, v106, vcc
	v_cmp_le_u32_e32 vcc, v51, v221
	v_or_b32_e32 v51, 0xd8, v227
	s_nop 0
	v_cndmask_b32_e32 v107, v50, v107, vcc
	v_cmp_le_u32_e32 vcc, v51, v221
	v_or_b32_e32 v51, 0xd9, v227
	s_nop 0
	v_cndmask_b32_e32 v108, v50, v108, vcc
	v_cmp_le_u32_e32 vcc, v51, v221
	v_or_b32_e32 v51, 0xda, v227
	s_nop 0
	v_cndmask_b32_e32 v109, v50, v109, vcc
	v_cmp_le_u32_e32 vcc, v51, v221
	s_nop 1
	v_cndmask_b32_e32 v110, v50, v110, vcc
	v_or_b32_e32 v50, 0xdb, v227
	v_cmp_gt_u32_e32 vcc, v50, v221
	s_and_saveexec_b64 s[2:3], vcc
	v_mov_b32_e32 v111, s8
	s_or_b64 exec, exec, s[2:3]

.LBB2_222:
	s_waitcnt lgkmcnt(14)
	s_cmp_lt_u32 s55, 4
	s_cbranch_scc1 .Lmsk_11606
	v_mfma_f32_32x32x16_f16 v[0:15], v[172:175], v[120:123], v[0:15]
.Lmsk_11606:
	v_exp_f32_e32 v96, v96
	v_exp_f32_e32 v97, v97
	v_exp_f32_e32 v98, v98
	v_exp_f32_e32 v99, v99
	s_waitcnt lgkmcnt(12)
	s_cmp_lt_u32 s55, 4
	s_cbranch_scc1 .Lmsk_11615
	v_mfma_f32_32x32x16_f16 v[16:31], v[172:175], v[116:119], v[16:31]
.Lmsk_11615:
	v_exp_f32_e32 v100, v100
	v_exp_f32_e32 v101, v101
	v_exp_f32_e32 v102, v102
	v_exp_f32_e32 v103, v103
	s_waitcnt lgkmcnt(10)
	s_cmp_lt_u32 s55, 4
	s_cbranch_scc1 .Lmsk_11624
	v_mfma_f32_32x32x16_f16 v[0:15], v[168:171], v[112:115], v[0:15]
.Lmsk_11624:
	v_exp_f32_e32 v104, v104
	v_exp_f32_e32 v105, v105
	v_exp_f32_e32 v106, v106
	v_exp_f32_e32 v107, v107
	s_waitcnt lgkmcnt(8)
	s_cmp_lt_u32 s55, 4
	s_cbranch_scc1 .Lmsk_11633
	v_mfma_f32_32x32x16_f16 v[16:31], v[168:171], v[88:91], v[16:31]
.Lmsk_11633:
	v_exp_f32_e32 v108, v108
	v_exp_f32_e32 v109, v109
	v_exp_f32_e32 v110, v110
	v_exp_f32_e32 v111, v111
	s_waitcnt lgkmcnt(6)
	s_cmp_lt_u32 s55, 5
	s_cbranch_scc1 .Lmsk_11642
	v_mfma_f32_32x32x16_f16 v[0:15], v[164:167], v[84:87], v[0:15]
.Lmsk_11642:
	v_exp_f32_e32 v32, v32
	v_exp_f32_e32 v33, v33
	v_exp_f32_e32 v34, v34
	v_exp_f32_e32 v35, v35
	s_waitcnt lgkmcnt(4)
	s_cmp_lt_u32 s55, 5
	s_cbranch_scc1 .Lmsk_11651
	v_mfma_f32_32x32x16_f16 v[16:31], v[164:167], v[80:83], v[16:31]
.Lmsk_11651:
	v_exp_f32_e32 v36, v36
	v_exp_f32_e32 v37, v37
	v_exp_f32_e32 v38, v38
	v_exp_f32_e32 v39, v39
	s_waitcnt lgkmcnt(2)
	s_cmp_lt_u32 s55, 5
	s_cbranch_scc1 .Lmsk_11660
	v_mfma_f32_32x32x16_f16 v[0:15], v[160:163], v[68:71], v[0:15]
.Lmsk_11660:
	v_exp_f32_e32 v40, v40
	v_exp_f32_e32 v41, v41
	v_exp_f32_e32 v42, v42
	v_exp_f32_e32 v43, v43
	s_waitcnt lgkmcnt(0)
	s_cmp_lt_u32 s55, 5
	s_cbranch_scc1 .Lmsk_11669
	v_mfma_f32_32x32x16_f16 v[16:31], v[160:163], v[64:67], v[16:31]
.Lmsk_11669:
	v_exp_f32_e32 v44, v44
	v_exp_f32_e32 v45, v45
	v_exp_f32_e32 v46, v46
	v_exp_f32_e32 v47, v47
	s_andn2_b64 vcc, exec, s[2:3]
	v_lshl_add_u32 v48, v227, 2, s24
	s_cbranch_vccnz .LBB2_224
	s_waitcnt lgkmcnt(0)
	ds_read_b128 v[50:53], v48 offset:49248
	ds_read_b128 v[54:57], v48 offset:49216
	ds_read_b128 v[58:61], v48 offset:49184
	ds_read_b128 v[62:65], v48 offset:49152
	s_waitcnt lgkmcnt(3)
	v_pk_mul_f32 v[14:15], v[14:15], v[52:53]
	s_waitcnt lgkmcnt(2)
	v_pk_mul_f32 v[10:11], v[10:11], v[56:57]
	s_waitcnt lgkmcnt(1)
	v_pk_mul_f32 v[6:7], v[6:7], v[60:61]
	s_waitcnt lgkmcnt(0)
	v_pk_mul_f32 v[2:3], v[2:3], v[64:65]
	v_pk_mul_f32 v[12:13], v[12:13], v[50:51]
	v_pk_mul_f32 v[8:9], v[8:9], v[54:55]
	v_pk_mul_f32 v[4:5], v[4:5], v[58:59]
	v_pk_mul_f32 v[0:1], v[0:1], v[62:63]
	v_pk_mul_f32 v[30:31], v[30:31], v[52:53]
	v_pk_mul_f32 v[26:27], v[26:27], v[56:57]
	v_pk_mul_f32 v[22:23], v[22:23], v[60:61]
	v_pk_mul_f32 v[18:19], v[18:19], v[64:65]
	v_pk_mul_f32 v[28:29], v[28:29], v[50:51]
	v_pk_mul_f32 v[24:25], v[24:25], v[54:55]
	v_pk_mul_f32 v[20:21], v[20:21], v[58:59]
	v_pk_mul_f32 v[16:17], v[16:17], v[62:63]
.LBB2_224:
	v_add_f32_e32 v49, v96, v97
	v_add_f32_e32 v49, v98, v49
	v_add_f32_e32 v49, v99, v49
	v_add_f32_e32 v49, v100, v49
	v_add_f32_e32 v49, v101, v49
	v_add_f32_e32 v49, v102, v49
	v_add_f32_e32 v49, v103, v49
	v_add_f32_e32 v49, v104, v49
	v_add_f32_e32 v49, v105, v49
	v_add_f32_e32 v49, v106, v49
	v_add_f32_e32 v49, v107, v49
	v_add_f32_e32 v49, v108, v49
	v_add_f32_e32 v49, v109, v49
	v_add_f32_e32 v49, v110, v49
	v_add_f32_e32 v49, v111, v49
	v_add_f32_e32 v49, v32, v49
	v_add_f32_e32 v49, v33, v49
	v_add_f32_e32 v49, v34, v49
	v_add_f32_e32 v49, v35, v49
	v_add_f32_e32 v49, v36, v49
	v_add_f32_e32 v49, v37, v49
	v_add_f32_e32 v49, v38, v49
	v_add_f32_e32 v49, v39, v49
	v_add_f32_e32 v49, v40, v49
	v_add_f32_e32 v49, v41, v49
	v_add_f32_e32 v49, v42, v49
	v_add_f32_e32 v49, v43, v49
	v_add_f32_e32 v49, v44, v49
	v_add_f32_e32 v49, v45, v49
	v_add_f32_e32 v49, v46, v49
	v_add_f32_e32 v49, v47, v49
	v_add_f32_e32 v49, v72, v49
	v_cvt_pk_f16_f32 v32, v32, v33
	v_cvt_pk_f16_f32 v50, v96, v97
	v_cvt_pk_f16_f32 v51, v98, v99
	v_cvt_pk_f16_f32 v52, v100, v101
	v_cvt_pk_f16_f32 v53, v102, v103
	v_cvt_pk_f16_f32 v54, v104, v105
	v_cvt_pk_f16_f32 v55, v106, v107
	v_cvt_pk_f16_f32 v56, v108, v109
	v_cvt_pk_f16_f32 v57, v110, v111
	v_cvt_pk_f16_f32 v33, v34, v35
	v_cvt_pk_f16_f32 v34, v36, v37
	v_cvt_pk_f16_f32 v35, v38, v39
	v_cvt_pk_f16_f32 v36, v40, v41
	v_cvt_pk_f16_f32 v37, v42, v43
	v_cvt_pk_f16_f32 v38, v44, v45
	v_cvt_pk_f16_f32 v39, v46, v47
	v_add_u32_e32 v70, s30, v228
	ds_read_b64_tr_b16 v[40:41],v70 offset:0
	ds_read_b64_tr_b16 v[42:43],v70 offset:512
	ds_read_b64_tr_b16 v[44:45],v70 offset:1024
	ds_read_b64_tr_b16 v[46:47],v70 offset:1536
	ds_read_b64_tr_b16 v[58:59],v70 offset:2048
	ds_read_b64_tr_b16 v[60:61],v70 offset:2560
	ds_read_b64_tr_b16 v[62:63],v70 offset:3072
	ds_read_b64_tr_b16 v[64:65],v70 offset:3584
	s_waitcnt lgkmcnt(0)
	s_nop 0
	s_cmp_lt_u32 s55, 6
	s_cbranch_scc1 .Lmsk_11788
	v_mfma_f32_32x32x16_f16 v[0:15], v[50:53], v[40:43], v[0:15]
.Lmsk_11788:
	ds_read_b64_tr_b16 v[40:41],v70 offset:4096
	ds_read_b64_tr_b16 v[42:43],v70 offset:4608
	s_cmp_lt_u32 s55, 6
	s_cbranch_scc1 .Lmsk_11795
	v_mfma_f32_32x32x16_f16 v[0:15], v[54:57], v[44:47], v[0:15]
.Lmsk_11795:
	ds_read_b64_tr_b16 v[44:45],v70 offset:5120
	ds_read_b64_tr_b16 v[46:47],v70 offset:5632
	s_cmp_lt_u32 s55, 7
	s_cbranch_scc1 .Lmsk_11802
	v_mfma_f32_32x32x16_f16 v[0:15], v[32:35], v[58:61], v[0:15]
.Lmsk_11802:
	ds_read_b64_tr_b16 v[58:59],v70 offset:6144
	ds_read_b64_tr_b16 v[60:61],v70 offset:6656
	ds_read_b64_tr_b16 v[66:67],v70 offset:7168
	ds_read_b64_tr_b16 v[68:69],v70 offset:7680
	s_waitcnt lgkmcnt(0)
	s_cmp_lt_u32 s55, 7
	s_cbranch_scc1 .Lmsk_11818
	v_mfma_f32_32x32x16_f16 v[0:15], v[36:39], v[62:65], v[0:15]
.Lmsk_11818:
	s_cmp_lt_u32 s55, 6
	s_cbranch_scc1 .Lmsk_11820
	v_mfma_f32_32x32x16_f16 v[16:31], v[50:53], v[40:43], v[16:31]
.Lmsk_11820:
	s_cmp_lt_u32 s55, 6
	s_cbranch_scc1 .Lmsk_11821
	v_mfma_f32_32x32x16_f16 v[16:31], v[54:57], v[44:47], v[16:31]
.Lmsk_11821:
	s_cmp_lt_u32 s55, 7
	s_cbranch_scc1 .Lmsk_11822
	v_mfma_f32_32x32x16_f16 v[16:31], v[32:35], v[58:61], v[16:31]
.Lmsk_11822:
	v_mov_b32_e32 v32, v49
	s_nop 1
	v_permlane32_swap_b32_e32 v49, v32
	s_cmp_lt_u32 s55, 7
	s_cbranch_scc1 .Lmsk_11826
	v_mfma_f32_32x32x16_f16 v[16:31], v[36:39], v[66:69], v[16:31]
.Lmsk_11826:
	s_and_saveexec_b64 s[2:3], s[0:1]
	v_add_f32_e32 v32, v49, v32
	ds_write_b32 v240, v32 offset:49280
	s_or_b64 exec, exec, s[2:3]
	s_waitcnt lgkmcnt(0)
	ds_read_b128 v[32:35], v48 offset:49280
	ds_read_b128 v[36:39], v48 offset:49312
	s_lshl_b64 s[0:1], s[4:5], 1
	s_add_u32 s0, s10, s0
	s_addc_u32 s1, s11, s1
	s_waitcnt lgkmcnt(1)
	v_rcp_f32_e32 v40, v32
	v_rcp_f32_e32 v41, v33
	s_lshl_b32 s2, s23, 12
	s_add_i32 s2, s2, 0
	v_rcp_f32_e32 v42, v34
	v_rcp_f32_e32 v43, v35
	s_waitcnt lgkmcnt(0)
	v_rcp_f32_e32 v44, v36
	ds_read_b128 v[32:35], v48 offset:49344
	v_rcp_f32_e32 v45, v37
	v_rcp_f32_e32 v46, v38
	v_rcp_f32_e32 v47, v39
	ds_read_b128 v[36:39], v48 offset:49376
	v_add3_u32 v48, s2, v230, v231
	v_fma_mixlo_f16 v0, v0, v40, 0
	ds_write_b16 v48, v0 offset:51200
	v_fma_mixlo_f16 v0, v16, v40, 0
	ds_write_b16 v48, v0 offset:51264
	v_fma_mixlo_f16 v0, v1, v41, 0
	ds_write_b16 v48, v0 offset:51328
	v_fma_mixlo_f16 v0, v17, v41, 0
	ds_write_b16 v48, v0 offset:51392
	v_fma_mixlo_f16 v0, v2, v42, 0
	ds_write_b16 v48, v0 offset:51456
	v_fma_mixlo_f16 v0, v18, v42, 0
	ds_write_b16 v48, v0 offset:51520
	v_fma_mixlo_f16 v0, v3, v43, 0
	ds_write_b16 v48, v0 offset:51584
	v_fma_mixlo_f16 v0, v19, v43, 0
	ds_write_b16 v48, v0 offset:51648
	v_fma_mixlo_f16 v0, v4, v44, 0
	ds_write_b16 v48, v0 offset:52224
	v_fma_mixlo_f16 v0, v20, v44, 0
	ds_write_b16 v48, v0 offset:52288
	v_fma_mixlo_f16 v0, v5, v45, 0
	ds_write_b16 v48, v0 offset:52352
	v_fma_mixlo_f16 v0, v21, v45, 0
	s_waitcnt lgkmcnt(12)
	v_rcp_f32_e32 v32, v32
	ds_write_b16 v48, v0 offset:52416
	v_fma_mixlo_f16 v0, v6, v46, 0
	ds_write_b16 v48, v0 offset:52480
	v_fma_mixlo_f16 v0, v22, v46, 0
	v_rcp_f32_e32 v33, v33
	ds_write_b16 v48, v0 offset:52544
	v_fma_mixlo_f16 v0, v7, v47, 0
	ds_write_b16 v48, v0 offset:52608
	v_fma_mixlo_f16 v0, v23, v47, 0
	v_rcp_f32_e32 v34, v34
	ds_write_b16 v48, v0 offset:52672
	v_fma_mixlo_f16 v0, v8, v32, 0
	ds_write_b16 v48, v0 offset:53248
	v_fma_mixlo_f16 v0, v24, v32, 0
	v_rcp_f32_e32 v35, v35
	ds_write_b16 v48, v0 offset:53312
	v_fma_mixlo_f16 v0, v9, v33, 0
	ds_write_b16 v48, v0 offset:53376
	v_fma_mixlo_f16 v0, v25, v33, 0
	s_waitcnt lgkmcnt(14)
	v_rcp_f32_e32 v36, v36
	ds_write_b16 v48, v0 offset:53440
	v_fma_mixlo_f16 v0, v10, v34, 0
	ds_write_b16 v48, v0 offset:53504
	v_fma_mixlo_f16 v0, v26, v34, 0
	v_rcp_f32_e32 v37, v37
	ds_write_b16 v48, v0 offset:53568
	v_fma_mixlo_f16 v0, v11, v35, 0
	ds_write_b16 v48, v0 offset:53632
	v_fma_mixlo_f16 v0, v27, v35, 0
	v_rcp_f32_e32 v38, v38
	ds_write_b16 v48, v0 offset:53696
	v_fma_mixlo_f16 v0, v12, v36, 0
	ds_write_b16 v48, v0 offset:54272
	v_fma_mixlo_f16 v0, v28, v36, 0
	v_rcp_f32_e32 v39, v39
	ds_write_b16 v48, v0 offset:54336
	v_fma_mixlo_f16 v0, v13, v37, 0
	ds_write_b16 v48, v0 offset:54400
	v_fma_mixlo_f16 v0, v29, v37, 0
	ds_write_b16 v48, v0 offset:54464
	v_fma_mixlo_f16 v0, v14, v38, 0
	ds_write_b16 v48, v0 offset:54528
	v_fma_mixlo_f16 v0, v30, v38, 0
	ds_write_b16 v48, v0 offset:54592
	v_fma_mixlo_f16 v0, v15, v39, 0
	ds_write_b16 v48, v0 offset:54656
	v_fma_mixlo_f16 v0, v31, v39, 0
	ds_write_b16 v48, v0 offset:54720
	v_add_u32_e32 v12, s2, v220
	s_waitcnt lgkmcnt(0)
	v_add_u32_e32 v0, v12, v232
	ds_read_b128 v[0:3], v0 offset:51200
	v_add_u32_e32 v4, v12, v233
	s_add_u32 s0, s0, s22
	ds_read_b128 v[4:7], v4 offset:51200
	s_addc_u32 s1, s1, 0
	v_mov_b32_e32 v221, 0
	v_lshl_add_u64 v[8:9], s[0:1], 0, v[220:221]
	v_lshlrev_b32_e32 v220, 1, v239
	v_lshl_add_u64 v[10:11], v[8:9], 0, v[220:221]
	v_lshlrev_b32_e32 v220, 1, v238
	s_waitcnt lgkmcnt(1)
	global_store_dwordx4 v[10:11], v[0:3], off sc1
	s_nop 1
	v_lshl_add_u64 v[0:1], v[8:9], 0, v[220:221]
	s_waitcnt lgkmcnt(0)
	global_store_dwordx4 v[0:1], v[4:7], off sc1
	v_add_u32_e32 v0, v12, v234
	ds_read_b128 v[0:3], v0 offset:51200
	v_add_u32_e32 v4, v12, v235
	ds_read_b128 v[4:7], v4 offset:51200
	v_lshlrev_b32_e32 v220, 1, v237
	v_lshl_add_u64 v[10:11], v[8:9], 0, v[220:221]
	v_lshlrev_b32_e32 v220, 1, v236
	s_waitcnt lgkmcnt(1)
	global_store_dwordx4 v[10:11], v[0:3], off sc1
	s_nop 1
	v_lshl_add_u64 v[0:1], v[8:9], 0, v[220:221]
	s_waitcnt lgkmcnt(0)
	global_store_dwordx4 v[0:1], v[4:7], off sc1
	s_waitcnt lgkmcnt(0)
	s_barrier
	s_endpgm

	.amdhsa_kernel _Z11attn_kernelPKDF16_S0_S0_PDF16_
		.amdhsa_group_segment_fixed_size 0
		.amdhsa_private_segment_fixed_size 0
		.amdhsa_kernarg_size 32
		.amdhsa_user_sgpr_count 2
		.amdhsa_user_sgpr_dispatch_ptr 0
		.amdhsa_user_sgpr_queue_ptr 0
		.amdhsa_user_sgpr_kernarg_segment_ptr 1
		.amdhsa_user_sgpr_dispatch_id 0
		.amdhsa_user_sgpr_kernarg_preload_length 0
		.amdhsa_user_sgpr_kernarg_preload_offset 0
		.amdhsa_user_sgpr_private_segment_size 0
		.amdhsa_uses_dynamic_stack 0
		.amdhsa_enable_private_segment 0
		.amdhsa_system_sgpr_workgroup_id_x 1
		.amdhsa_system_sgpr_workgroup_id_y 0
		.amdhsa_system_sgpr_workgroup_id_z 0
		.amdhsa_system_sgpr_workgroup_info 0
		.amdhsa_system_vgpr_workitem_id 0
		.amdhsa_next_free_vgpr 243
		.amdhsa_next_free_sgpr 56
		.amdhsa_accum_offset 244
		.amdhsa_reserve_vcc 1
		.amdhsa_float_round_mode_32 0
		.amdhsa_float_round_mode_16_64 0
		.amdhsa_float_denorm_mode_32 3
		.amdhsa_float_denorm_mode_16_64 3
		.amdhsa_dx10_clamp 1
		.amdhsa_ieee_mode 1
		.amdhsa_fp16_overflow 0
		.amdhsa_tg_split 0
		.amdhsa_exception_fp_ieee_invalid_op 0
		.amdhsa_exception_fp_denorm_src 0
		.amdhsa_exception_fp_ieee_div_zero 0
		.amdhsa_exception_fp_ieee_overflow 0
		.amdhsa_exception_fp_ieee_underflow 0
		.amdhsa_exception_fp_ieee_inexact 0
		.amdhsa_exception_int_div_zero 0
	.end_amdhsa_kernel

amdhsa.kernels:
  - .agpr_count:     0
    .args:
      - .actual_access:  read_only
        .address_space:  global
        .offset:         0
        .size:           8
        .value_kind:     global_buffer
      - .actual_access:  read_only
        .address_space:  global
        .offset:         8
        .size:           8
        .value_kind:     global_buffer
      - .actual_access:  read_only
        .address_space:  global
        .offset:         16
        .size:           8
        .value_kind:     global_buffer
      - .actual_access:  read_only
        .address_space:  global
        .offset:         24
        .size:           8
        .value_kind:     global_buffer
      - .actual_access:  read_only
        .address_space:  global
        .offset:         32
        .size:           8
        .value_kind:     global_buffer
      - .actual_access:  read_only
        .address_space:  global
        .offset:         40
        .size:           8
        .value_kind:     global_buffer
      - .address_space:  global
        .offset:         48
        .size:           8
        .value_kind:     global_buffer
      - .address_space:  global
        .offset:         56
        .size:           8
        .value_kind:     global_buffer
      - .address_space:  global
        .offset:         64
        .size:           8
        .value_kind:     global_buffer
      - .address_space:  global
        .offset:         72
        .size:           8
        .value_kind:     global_buffer
    .group_segment_fixed_size: 0
    .kernarg_segment_align: 8
    .kernarg_segment_size: 80
    .language:       OpenCL C
    .language_version:
      - 2
      - 0
    .max_flat_workgroup_size: 256
    .name:           _Z11prep_kernelPKfPKiS0_S0_S0_S0_PtS3_S3_P15HIP_vector_typeIfLj2EE
    .private_segment_fixed_size: 0
    .sgpr_count:     40
    .sgpr_spill_count: 0
    .symbol:         _Z11prep_kernelPKfPKiS0_S0_S0_S0_PtS3_S3_P15HIP_vector_typeIfLj2EE.kd
    .uniform_work_group_size: 1
    .uses_dynamic_stack: false
    .vgpr_count:     40
    .vgpr_spill_count: 0
    .wavefront_size: 64
  - .agpr_count:     0
    .args:
      - .offset:         0
        .size:           32
        .value_kind:     by_value
      - .offset:         32
        .size:           24
        .value_kind:     by_value
      - .offset:         56
        .size:           32
        .value_kind:     by_value
      - .offset:         88
        .size:           24
        .value_kind:     by_value
      - .offset:         112
        .size:           4
        .value_kind:     hidden_block_count_x
      - .offset:         116
        .size:           4
        .value_kind:     hidden_block_count_y
      - .offset:         120
        .size:           4
        .value_kind:     hidden_block_count_z
      - .offset:         124
        .size:           2
        .value_kind:     hidden_group_size_x
      - .offset:         126
        .size:           2
        .value_kind:     hidden_group_size_y
      - .offset:         128
        .size:           2
        .value_kind:     hidden_group_size_z
      - .offset:         130
        .size:           2
        .value_kind:     hidden_remainder_x
      - .offset:         132
        .size:           2
        .value_kind:     hidden_remainder_y
      - .offset:         134
        .size:           2
        .value_kind:     hidden_remainder_z
      - .offset:         152
        .size:           8
        .value_kind:     hidden_global_offset_x
      - .offset:         160
        .size:           8
        .value_kind:     hidden_global_offset_y
      - .offset:         168
        .size:           8
        .value_kind:     hidden_global_offset_z
      - .offset:         176
        .size:           2
        .value_kind:     hidden_grid_dims
      - .offset:         232
        .size:           4
        .value_kind:     hidden_dynamic_lds_size
    .group_segment_fixed_size: 0
    .kernarg_segment_align: 8
    .kernarg_segment_size: 368
    .language:       OpenCL C
    .language_version:
      - 2
      - 0
    .max_flat_workgroup_size: 512
    .name:           _Z10qkv_kernelN3pg84GemmENS_7EpiRopeEN2hg4GemmENS2_7EpiRopeE
    .private_segment_fixed_size: 0
    .sgpr_count:     99
    .sgpr_spill_count: 0
    .symbol:         _Z10qkv_kernelN3pg84GemmENS_7EpiRopeEN2hg4GemmENS2_7EpiRopeE.kd
    .uniform_work_group_size: 1
    .uses_dynamic_stack: false
    .vgpr_count:     240
    .vgpr_spill_count: 0
    .wavefront_size: 64
  - .agpr_count:     0
    .args:
      - .address_space:  global
        .offset:         0
        .size:           8
        .value_kind:     global_buffer
      - .address_space:  global
        .offset:         8
        .size:           8
        .value_kind:     global_buffer
      - .address_space:  global
        .offset:         16
        .size:           8
        .value_kind:     global_buffer
      - .address_space:  global
        .offset:         24
        .size:           8
        .value_kind:     global_buffer
    .group_segment_fixed_size: 0
    .kernarg_segment_align: 8
    .kernarg_segment_size: 32
    .language:       OpenCL C
    .language_version:
      - 2
      - 0
    .max_flat_workgroup_size: 512
    .name:           _Z11attn_kernelPKDF16_S0_S0_PDF16_
    .private_segment_fixed_size: 0
    .sgpr_count:     62
    .sgpr_spill_count: 0
    .symbol:         _Z11attn_kernelPKDF16_S0_S0_PDF16_.kd
    .uniform_work_group_size: 1
    .uses_dynamic_stack: false
    .vgpr_count:     243
    .vgpr_spill_count: 0
    .wavefront_size: 64
  - .agpr_count:     0
    .args:
      - .offset:         0
        .size:           32
        .value_kind:     by_value
      - .offset:         32
        .size:           16
        .value_kind:     by_value
      - .offset:         48
        .size:           4
        .value_kind:     hidden_block_count_x
      - .offset:         52
        .size:           4
        .value_kind:     hidden_block_count_y
      - .offset:         56
        .size:           4
        .value_kind:     hidden_block_count_z
      - .offset:         60
        .size:           2
        .value_kind:     hidden_group_size_x
      - .offset:         62
        .size:           2
        .value_kind:     hidden_group_size_y
      - .offset:         64
        .size:           2
        .value_kind:     hidden_group_size_z
      - .offset:         66
        .size:           2
        .value_kind:     hidden_remainder_x
      - .offset:         68
        .size:           2
        .value_kind:     hidden_remainder_y
      - .offset:         70
        .size:           2
        .value_kind:     hidden_remainder_z
      - .offset:         88
        .size:           8
        .value_kind:     hidden_global_offset_x
      - .offset:         96
        .size:           8
        .value_kind:     hidden_global_offset_y
      - .offset:         104
        .size:           8
        .value_kind:     hidden_global_offset_z
      - .offset:         112
        .size:           2
        .value_kind:     hidden_grid_dims
      - .offset:         168
        .size:           4
        .value_kind:     hidden_dynamic_lds_size
    .group_segment_fixed_size: 0
    .kernarg_segment_align: 8
    .kernarg_segment_size: 304
    .language:       OpenCL C
    .language_version:
      - 2
      - 0
    .max_flat_workgroup_size: 512
    .name:           _Z12hgemm_kernelIN2hg6EpiF32EEvNS0_4GemmET_
    .private_segment_fixed_size: 0
    .sgpr_count:     62
    .sgpr_spill_count: 0
    .symbol:         _Z12hgemm_kernelIN2hg6EpiF32EEvNS0_4GemmET_.kd
    .uniform_work_group_size: 1
    .uses_dynamic_stack: false
    .vgpr_count:     138
    .vgpr_spill_count: 0
    .wavefront_size: 64
